# h0_phase: 16 row-segment loads batched per iteration with counted vmcnt (was load-wait-store serialized); plus mod_phase pipelining; on top of v28
# baseline (speedup 1.0000x reference)
.Lh0_loop:
	v_lshl_add_u64 v[42:43], v[34:35], 0, s[0:1]
	global_load_dwordx4 v[48:51], v[42:43], off
	global_load_dwordx4 v[52:55], v[42:43], off offset:1024
	global_load_dwordx4 v[56:59], v[42:43], off offset:2048
	global_load_dwordx4 v[60:63], v[42:43], off offset:3072
	v_lshl_add_u64 v[44:45], v[42:43], 0, s[4:5]
	global_load_dwordx4 v[64:67], v[44:45], off
	global_load_dwordx4 v[68:71], v[44:45], off offset:1024
	global_load_dwordx4 v[72:75], v[44:45], off offset:2048
	global_load_dwordx4 v[76:79], v[44:45], off offset:3072
	v_lshl_add_u64 v[46:47], v[44:45], 0, s[4:5]
	global_load_dwordx4 v[80:83], v[46:47], off
	global_load_dwordx4 v[84:87], v[46:47], off offset:1024
	global_load_dwordx4 v[88:91], v[46:47], off offset:2048
	global_load_dwordx4 v[92:95], v[46:47], off offset:3072
	v_lshl_add_u64 v[42:43], v[46:47], 0, s[4:5]
	global_load_dwordx4 v[96:99], v[42:43], off
	global_load_dwordx4 v[100:103], v[42:43], off offset:1024
	global_load_dwordx4 v[104:107], v[42:43], off offset:2048
	global_load_dwordx4 v[108:111], v[42:43], off offset:3072
	s_add_u32 s0, s0, 0x4000
	s_addc_u32 s1, s1, 0
	s_waitcnt vmcnt(15)
	v_pk_fma_f32 v[48:49], v[6:7], v[48:49], v[2:3]
	v_pk_fma_f32 v[50:51], v[8:9], v[50:51], v[4:5]
	v_mov_b32_e32 v176, 0
	v_cvt_pk_fp8_f32 v176, v48, v49
	s_nop 0
	v_cvt_pk_fp8_f32 v176, v50, v51 op_sel:[0,0,1]
	global_store_dword v[36:37], v176, off offset:-2048
	s_waitcnt vmcnt(15)
	v_pk_fma_f32 v[52:53], v[18:19], v[52:53], v[10:11]
	v_pk_fma_f32 v[54:55], v[20:21], v[54:55], v[12:13]
	v_mov_b32_e32 v177, 0
	v_cvt_pk_fp8_f32 v177, v52, v53
	s_nop 0
	v_cvt_pk_fp8_f32 v177, v54, v55 op_sel:[0,0,1]
	global_store_dword v[36:37], v177, off offset:-1792
	s_waitcnt vmcnt(15)
	v_pk_fma_f32 v[56:57], v[26:27], v[56:57], v[14:15]
	v_pk_fma_f32 v[58:59], v[28:29], v[58:59], v[16:17]
	v_mov_b32_e32 v178, 0
	v_cvt_pk_fp8_f32 v178, v56, v57
	s_nop 0
	v_cvt_pk_fp8_f32 v178, v58, v59 op_sel:[0,0,1]
	global_store_dword v[36:37], v178, off offset:-1536
	s_waitcnt vmcnt(15)
	v_pk_fma_f32 v[60:61], v[30:31], v[60:61], v[22:23]
	v_pk_fma_f32 v[62:63], v[32:33], v[62:63], v[24:25]
	v_mov_b32_e32 v179, 0
	v_cvt_pk_fp8_f32 v179, v60, v61
	s_nop 0
	v_cvt_pk_fp8_f32 v179, v62, v63 op_sel:[0,0,1]
	global_store_dword v[36:37], v179, off offset:-1280
	s_waitcnt vmcnt(15)
	v_pk_fma_f32 v[64:65], v[6:7], v[64:65], v[2:3]
	v_pk_fma_f32 v[66:67], v[8:9], v[66:67], v[4:5]
	v_mov_b32_e32 v180, 0
	v_cvt_pk_fp8_f32 v180, v64, v65
	s_nop 0
	v_cvt_pk_fp8_f32 v180, v66, v67 op_sel:[0,0,1]
	global_store_dword v[36:37], v180, off offset:-1024
	s_waitcnt vmcnt(15)
	v_pk_fma_f32 v[68:69], v[18:19], v[68:69], v[10:11]
	v_pk_fma_f32 v[70:71], v[20:21], v[70:71], v[12:13]
	v_mov_b32_e32 v181, 0
	v_cvt_pk_fp8_f32 v181, v68, v69
	s_nop 0
	v_cvt_pk_fp8_f32 v181, v70, v71 op_sel:[0,0,1]
	global_store_dword v[36:37], v181, off offset:-768
	s_waitcnt vmcnt(15)
	v_pk_fma_f32 v[72:73], v[26:27], v[72:73], v[14:15]
	v_pk_fma_f32 v[74:75], v[28:29], v[74:75], v[16:17]
	v_mov_b32_e32 v182, 0
	v_cvt_pk_fp8_f32 v182, v72, v73
	s_nop 0
	v_cvt_pk_fp8_f32 v182, v74, v75 op_sel:[0,0,1]
	global_store_dword v[36:37], v182, off offset:-512
	s_waitcnt vmcnt(15)
	v_pk_fma_f32 v[76:77], v[30:31], v[76:77], v[22:23]
	v_pk_fma_f32 v[78:79], v[32:33], v[78:79], v[24:25]
	v_mov_b32_e32 v183, 0
	v_cvt_pk_fp8_f32 v183, v76, v77
	s_nop 0
	v_cvt_pk_fp8_f32 v183, v78, v79 op_sel:[0,0,1]
	global_store_dword v[36:37], v183, off offset:-256
	s_waitcnt vmcnt(15)
	v_pk_fma_f32 v[80:81], v[6:7], v[80:81], v[2:3]
	v_pk_fma_f32 v[82:83], v[8:9], v[82:83], v[4:5]
	v_mov_b32_e32 v184, 0
	v_cvt_pk_fp8_f32 v184, v80, v81
	s_nop 0
	v_cvt_pk_fp8_f32 v184, v82, v83 op_sel:[0,0,1]
	global_store_dword v[36:37], v184, off
	s_waitcnt vmcnt(15)
	v_pk_fma_f32 v[84:85], v[18:19], v[84:85], v[10:11]
	v_pk_fma_f32 v[86:87], v[20:21], v[86:87], v[12:13]
	v_mov_b32_e32 v185, 0
	v_cvt_pk_fp8_f32 v185, v84, v85
	s_nop 0
	v_cvt_pk_fp8_f32 v185, v86, v87 op_sel:[0,0,1]
	global_store_dword v[36:37], v185, off offset:256
	s_waitcnt vmcnt(15)
	v_pk_fma_f32 v[88:89], v[26:27], v[88:89], v[14:15]
	v_pk_fma_f32 v[90:91], v[28:29], v[90:91], v[16:17]
	v_mov_b32_e32 v186, 0
	v_cvt_pk_fp8_f32 v186, v88, v89
	s_nop 0
	v_cvt_pk_fp8_f32 v186, v90, v91 op_sel:[0,0,1]
	global_store_dword v[36:37], v186, off offset:512
	s_waitcnt vmcnt(15)
	v_pk_fma_f32 v[92:93], v[30:31], v[92:93], v[22:23]
	v_pk_fma_f32 v[94:95], v[32:33], v[94:95], v[24:25]
	v_mov_b32_e32 v187, 0
	v_cvt_pk_fp8_f32 v187, v92, v93
	s_nop 0
	v_cvt_pk_fp8_f32 v187, v94, v95 op_sel:[0,0,1]
	global_store_dword v[36:37], v187, off offset:768
	s_waitcnt vmcnt(15)
	v_pk_fma_f32 v[96:97], v[6:7], v[96:97], v[2:3]
	v_pk_fma_f32 v[98:99], v[8:9], v[98:99], v[4:5]
	v_mov_b32_e32 v188, 0
	v_cvt_pk_fp8_f32 v188, v96, v97
	s_nop 0
	v_cvt_pk_fp8_f32 v188, v98, v99 op_sel:[0,0,1]
	global_store_dword v[36:37], v188, off offset:1024
	s_waitcnt vmcnt(15)
	v_pk_fma_f32 v[100:101], v[18:19], v[100:101], v[10:11]
	v_pk_fma_f32 v[102:103], v[20:21], v[102:103], v[12:13]
	v_mov_b32_e32 v189, 0
	v_cvt_pk_fp8_f32 v189, v100, v101
	s_nop 0
	v_cvt_pk_fp8_f32 v189, v102, v103 op_sel:[0,0,1]
	global_store_dword v[36:37], v189, off offset:1280
	s_waitcnt vmcnt(15)
	v_pk_fma_f32 v[104:105], v[26:27], v[104:105], v[14:15]
	v_pk_fma_f32 v[106:107], v[28:29], v[106:107], v[16:17]
	v_mov_b32_e32 v190, 0
	v_cvt_pk_fp8_f32 v190, v104, v105
	s_nop 0
	v_cvt_pk_fp8_f32 v190, v106, v107 op_sel:[0,0,1]
	global_store_dword v[36:37], v190, off offset:1536
	s_waitcnt vmcnt(15)
	v_pk_fma_f32 v[108:109], v[30:31], v[108:109], v[22:23]
	v_pk_fma_f32 v[110:111], v[32:33], v[110:111], v[24:25]
	v_mov_b32_e32 v191, 0
	v_cvt_pk_fp8_f32 v191, v108, v109
	s_nop 0
	v_cvt_pk_fp8_f32 v191, v110, v111 op_sel:[0,0,1]
	global_store_dword v[36:37], v191, off offset:1792
	v_lshl_add_u64 v[36:37], v[36:37], 0, s[4:5]
	s_cmp_lg_u32 s0, 0x10000
	s_cbranch_scc1 .Lh0_loop
	s_getreg_b32 s3, hwreg(HW_REG_XCC_ID, 0, 4)
	s_waitcnt vmcnt(0)
	s_barrier
	s_mov_b64 s[0:1], exec
	v_readlane_b32 s4, v254, 5
	v_readlane_b32 s5, v254, 6
	s_and_b64 s[4:5], s[0:1], s[4:5]
	s_xor_b64 s[0:1], s[4:5], s[0:1]
	s_mov_b64 exec, s[4:5]
	s_cbranch_execz .LBB0_213
	s_add_i32 s4, 0, 0x20160
	v_mov_b32_e32 v1, s4
	s_waitcnt vmcnt(0) expcnt(0) lgkmcnt(0)
	ds_read_b32 v3, v1
	s_add_i32 s4, 0, 0x20164
	v_mov_b32_e32 v1, s4
	ds_read_b32 v1, v1
	s_and_b32 s3, s3, 15
	s_waitcnt lgkmcnt(1)
	v_cmp_ne_u32_e32 vcc, 0, v3
	s_cbranch_vccnz .LBB0_176
	v_readlane_b32 s4, v254, 3
	v_readlane_b32 s5, v254, 4
	s_load_dwordx2 s[8:9], s[4:5], 0x4
	s_add_u32 s4, s64, 0x39801200
	s_addc_u32 s5, s65, 0
	s_add_u32 s6, s64, 0x39801400
	s_addc_u32 s7, s65, 0
	v_readlane_b32 s10, v254, 0
	s_waitcnt lgkmcnt(0)
	s_mul_i32 s33, s8, s10
	s_add_u32 s8, s64, 0x39801500
	s_mul_i32 s33, s33, s9
	s_addc_u32 s9, s65, 0
	s_add_u32 s10, s64, 0x39801600
	s_addc_u32 s11, s65, 0
	s_add_u32 s12, s64, 0x39801700
	s_addc_u32 s13, s65, 0
	s_add_u32 s14, s64, 0x39801800
	s_addc_u32 s15, s65, 0
	s_add_u32 s16, s64, 0x39801900
	s_addc_u32 s17, s65, 0
	s_add_u32 s18, s64, 0x39801a00
	s_addc_u32 s19, s65, 0
	s_add_u32 s20, s64, 0x39801b00
	s_addc_u32 s21, s65, 0
	s_add_u32 s22, s64, 0x39801c00
	s_addc_u32 s23, s65, 0
	s_add_u32 s24, s64, 0x39801d00
	s_addc_u32 s25, s65, 0
	s_add_u32 s26, s64, 0x39801e00
	s_addc_u32 s27, s65, 0
	s_add_u32 s28, s64, 0x39801f00
	s_addc_u32 s29, s65, 0
	s_add_u32 s30, s64, 0x39802000
	s_addc_u32 s31, s65, 0
	s_add_u32 s34, s64, 0x39802100
	s_addc_u32 s35, s65, 0
	s_add_u32 s36, s64, 0x39802200
	s_addc_u32 s37, s65, 0
	s_add_u32 s38, s64, 0x39802300
	s_addc_u32 s39, s65, 0
	s_mov_b32 s46, 1
	v_mov_b32_e32 v17, 0
	s_branch .LBB0_164
